# v9 + P2 per-XCD K-stagger with a 2-K-tile step per XCD (start K-tile 2x instead of 4x)
# baseline (speedup 1.0000x reference)
;     __device__ bool next(int i, Unit& u) const { if (!StaticOrder::next(i >> 1, u)) return false; u.kh = i & 1; return true; }
;     __device__ bool next(int i, Unit& u) const { if (i >= 2) return false; u.pm = 0; u.pn = 0; u.e = 0; u.kh = 0; return true; }
;     __device__ bool next(int i, Unit& u) const { if (!StaticOrder::next(i, u)) return false; u.e = tile_e[u.pm]; return true; }
; #define PG8_STAGE(bufoff, gbase, voff) do { _Pragma("unroll") for (int _i = 0; _i < 2; ++_i) \
;         __builtin_amdgcn_global_load_lds((const unsigned*)((const char*)(gbase) + (voff)[_i]), (PG8_LAS unsigned*)(lds + (bufoff) + ldsw + _i * 8192), 16, 0, 0); } while (0)
; #define PG8_WAIT_V(n) asm volatile("s_waitcnt vmcnt(" #n ")" ::: "memory")
; #define PG8_BAR __builtin_amdgcn_s_barrier()
;     __host__ __device__ bool next(int i, Unit& u) const {
;         const long L = (long)i * G + c; if (L >= nwg) return false;
;         int wgid = (int)L; { const int q = nwg / NXCD, r = nwg % NXCD, xcd = wgid % NXCD, off = wgid / NXCD; wgid = (xcd < r ? xcd * (q + 1) : r * (q + 1) + (xcd - r) * q) + off; }
;         const int nig = WGM * nN, gid = wgid / nig, fm = gid * WGM, gsz = (nM - fm) < WGM ? (nM - fm) : WGM;
;         u.pm = fm + ((wgid % nig) % gsz); u.pn = (wgid % nig) / gsz; u.e = 0; u.kh = 0; return true;
; template <class Epi, class Sched, bool ALIGN_EPI = false, bool SP2 = false, bool GATHER = false, bool F8 = false>
; __device__ __forceinline__ void gemm_phase(PG8_LAS unsigned char* lds, const Gemm g, const Sched& S, const Epi& E) {
;     ...
;     const char* cA = (const char*)((Sched::PAIRS && cur.kh) ? g.A2 : g.A) + (GATHER ? (size_t)0 : (size_t)cur.pm * tstep); const char* cB = (const char*)((Sched::PAIRS && cur.kh) ? g.Bt2 : g.Bt) + (size_t)cur.e * g.bgs + (size_t)cur.pn * tstep;
;     S.a_ready(cur);
;     if constexpr (GATHER) load_gather(cur, gc0, gc1);
;     if constexpr (SP2) {
;         PG8_STAGE(PG8_SB(0, 0), cB, voffB); PG8_STAGE(PG8_SB(0, 1), cB + hstep, voffB); PG8_STAGE_A(PG8_SA(0, 0), cA, 0, false); PG8_STAGE_A(PG8_SA(0, 1), cA, 1, false);
;         if (wr == 1) PG8_BAR;
;         PG8_WAIT_V(2); PG8_BAR;
;         PG8_STAGE(PG8_SB(1, 0), cB + kstep, voffB); PG8_STAGE_A(PG8_SA(1, 0), cA + kstep, 0, false); PG8_STAGE(PG8_SB(1, 1), cB + hstep + kstep, voffB);
;         PG8_WAIT_V(6); PG8_BAR;
.LBB0_290:
	s_add_u32 s34, s50, 0x39000000
	s_addc_u32 s35, s51, 0
	s_cmp_lt_i32 s24, 3
	s_cselect_b64 s[0:1], -1, 0
	s_cmp_gt_i32 s25, 2
	s_cselect_b64 s[2:3], -1, 0
	s_and_b64 s[0:1], s[0:1], s[2:3]
	s_andn2_b64 vcc, exec, s[0:1]
	s_cbranch_vccnz .LBB0_480
	s_cmpk_eq_i32 s93, 0x100
	s_cselect_b64 s[4:5], -1, 0
	s_cmpk_lg_i32 s93, 0x100
	v_readlane_b32 s0, v253, 2
	s_cselect_b64 s[8:9], -1, 0
	s_cmpk_gt_i32 s0, 0xe7
	s_cselect_b64 s[0:1], -1, 0
	s_and_b64 s[0:1], s[0:1], s[4:5]
	v_lshlrev_b32_e32 v154, 4, v0
	s_and_b64 vcc, exec, s[0:1]
	s_cbranch_vccnz .LBB0_308
	v_readlane_b32 s2, v253, 2
	s_cmpk_gt_i32 s2, 0xb7f
	v_readfirstlane_b32 s15, v0
	s_cbranch_scc1 .LBB0_308
	v_and_b32_e32 v1, 32, v0
	s_waitcnt vmcnt(9)
	v_bitop3_b32 v10, v154, v1, 48 bitop3:0x6c
	v_bfe_u32 v11, v0, 2, 4
	v_lshrrev_b32_e32 v2, 1, v10
	v_lshrrev_b32_e32 v1, 1, v0
	v_bfe_u32 v3, v0, 2, 2
	v_lshrrev_b32_e32 v4, 3, v0
	v_lshrrev_b32_e32 v7, 5, v0
	v_and_or_b32 v3, v1, 24, v3
	v_and_or_b32 v5, v4, 48, v11
	v_and_or_b32 v6, v1, 32, v2
	v_and_or_b32 v4, v4, 32, v7
	s_lshr_b32 s12, s15, 6
	v_and_or_b32 v4, v4, 36, v3
	v_lshlrev_b32_e32 v6, 1, v6
	v_or_b32_e32 v12, 0x2000, v154
	s_lshr_b32 s16, s15, 8
	s_lshl_b32 s2, s12, 10
	v_lshl_or_b32 v130, v5, 12, v6
	v_lshl_or_b32 v132, v4, 12, v6
	v_lshrrev_b32_e32 v4, 7, v12
	s_movk_i32 s10, 0x70
	v_lshrrev_b32_e32 v6, 5, v154
	s_add_u32 s3, s50, 0x1200000
	v_and_or_b32 v5, v4, s10, v11
	v_and_or_b32 v2, v6, 32, v2
	v_lshrrev_b32_e32 v6, 9, v154
	s_movk_i32 s10, 0x60
	v_readlane_b32 s13, v253, 2
	s_addc_u32 s20, s51, 0
	v_and_or_b32 v4, v4, s10, v6
	s_movk_i32 s10, 0x64
	s_ashr_i32 s21, s13, 31
	v_and_or_b32 v3, v4, s10, v3
	s_lshr_b32 s10, s21, 29
	s_add_i32 s10, s13, s10
	s_ashr_i32 s11, s10, 3
	s_and_b32 s10, s10, -8
	s_sub_i32 s10, s13, s10
	s_cmp_lt_i32 s10, 0
	s_movk_i32 s22, 0x171
	s_cselect_b32 s13, s22, 0x170
	s_mul_i32 s10, s10, s13
	s_add_i32 s10, s10, s11
	s_mul_hi_i32 s11, s10, 0xb21642c9
	s_add_i32 s11, s11, s10
	s_lshr_b32 s13, s11, 31
	s_ashr_i32 s11, s11, 8
	s_add_i32 s11, s11, s13
	s_lshl_b32 s13, s11, 3
	s_mulk_i32 s11, 0x170
	s_sub_i32 s10, s10, s11
	s_sext_i32_i16 s11, s10
	s_bfe_u32 s11, s11, 0x3001c
	s_add_i32 s11, s10, s11
	s_sext_i32_i16 s14, s11
	s_and_b32 s11, s11, 0xfff8
	s_sub_i32 s10, s10, s11
	s_sext_i32_i16 s10, s10
	s_lshr_b32 s14, s14, 3
	v_readlane_b32 s100, v253, 2
	s_and_b32 s100, s100, 7
	s_mul_i32 s100, s100, 6
	s_add_i32 s14, s14, s100
	s_cmp_ge_i32 s14, 46
	s_cselect_b32 s101, 46, 0
	s_sub_i32 s14, s14, s101
	s_add_i32 s58, s13, s10
	s_ashr_i32 s59, s58, 31
	v_readlane_b32 s98, v253, 2
	s_and_b32 s98, s98, 7
	s_lshl_b32 s99, s98, 8
	s_lshl_b32 s98, s98, 1
	s_sub_i32 s98, 28, s98
	s_bfe_i64 s[18:19], s[14:15], 0x100000
	s_lshl_b64 s[10:11], s[58:59], 20
	s_lshl_b64 s[18:19], s[18:19], 20
	s_add_u32 s64, s3, s18
	s_addc_u32 s65, s20, s19
	s_add_u32 s64, s64, s99
	s_addc_u32 s65, s65, 0
	s_add_i32 s23, s2, 0
	s_add_i32 m0, s23, 0x10000
	v_lshlrev_b32_e32 v2, 1, v2
	global_load_lds_dwordx4 v132, s[64:65]
	s_add_i32 m0, s23, 0x12000
	v_lshl_or_b32 v136, v3, 12, v2
	s_add_u32 s18, s64, 0x80000
	global_load_lds_dwordx4 v136, s[64:65]
	s_addc_u32 s19, s65, 0
	s_add_i32 m0, s23, 0x14000
	v_lshl_or_b32 v134, v5, 12, v2
	global_load_lds_dwordx4 v132, s[18:19]
	s_add_i32 m0, s23, 0x16000
	s_add_u32 s60, s6, s10
	s_addc_u32 s61, s7, s11
	s_add_u32 s60, s60, s99
	s_addc_u32 s61, s61, 0
	s_add_i32 s24, s23, 0x2000
	global_load_lds_dwordx4 v136, s[18:19]
	s_mov_b32 m0, s23
	s_add_u32 s10, s60, 0x80000
	global_load_lds_dwordx4 v130, s[60:61]
	s_mov_b32 m0, s24
	s_addc_u32 s11, s61, 0
	s_add_i32 s25, s23, 0x4000
	global_load_lds_dwordx4 v134, s[60:61]
	s_mov_b32 m0, s25
	s_add_i32 s26, s23, 0x6000
	global_load_lds_dwordx4 v130, s[10:11]
	s_mov_b32 m0, s26
	v_mov_b32_e32 v133, 0
	global_load_lds_dwordx4 v134, s[10:11]
	v_mov_b32_e32 v137, v133
	v_mov_b32_e32 v131, v133
	v_mov_b32_e32 v135, v133
	s_cmp_eq_u32 s16, 1
	s_mov_b32 s27, 0
	v_lshl_add_u64 v[8:9], s[64:65], 0, v[132:133]
	v_lshl_add_u64 v[6:7], s[64:65], 0, v[136:137]
	v_lshl_add_u64 v[2:3], s[60:61], 0, v[130:131]
	s_cselect_b64 s[10:11], -1, 0
	s_cmp_lg_u32 s16, 1
	v_lshl_add_u64 v[4:5], s[60:61], 0, v[134:135]
	s_cbranch_scc1 .LBB0_295
	s_barrier

;     __device__ bool next(int i, Unit& u) const { if (!StaticOrder::next(i >> 1, u)) return false; u.kh = i & 1; return true; }
;     __device__ bool next(int i, Unit& u) const { if (i >= 2) return false; u.pm = 0; u.pn = 0; u.e = 0; u.kh = 0; return true; }
;     __device__ bool next(int i, Unit& u) const { if (!StaticOrder::next(i, u)) return false; u.e = tile_e[u.pm]; return true; }
; template <class Epi, class Sched, bool ALIGN_EPI = false, bool SP2 = false, bool GATHER = false, bool F8 = false>
; __device__ __forceinline__ void gemm_phase(PG8_LAS unsigned char* lds, const Gemm g, const Sched& S, const Epi& E) {
;     ...
;         const bool has_next = S.next(ui + 1, nxt);
;         const char* nA = has_next ? (const char*)((Sched::PAIRS && nxt.kh) ? g.A2 : g.A) + (GATHER ? (size_t)0 : (size_t)nxt.pm * tstep) : cA;
;         if constexpr (GATHER) { if (has_next) load_gather(nxt, gn0, gn1); else { gn0[0] = gc0[0]; gn0[1] = gc0[1]; gn1[0] = gc1[0]; gn1[1] = gc1[1]; } } const char* nB = has_next ? (const char*)((Sched::PAIRS && nxt.kh) ? g.Bt2 : g.Bt) + (size_t)nxt.e * g.bgs + (size_t)nxt.pn * tstep : cB;
;         for (int t = 0; t < nt; t += 2) {
;             const bool last = (t == nt - 2);
;             const char* a1 = cA + (size_t)(t + 1) * kstep;
;             const char* a2 = last ? nA : cA + (size_t)(t + 2) * kstep; const char* b2 = last ? nB : cB + (size_t)(t + 2) * kstep;
;             const char* a3 = a2 + kstep; const char* b3 = b2 + kstep;
;     ...
; #pragma unroll
;         for (int a = 0; a < 2; ++a)
; #pragma unroll
;             for (int b = 0; b < 2; ++b)
; #pragma unroll
;                 for (int m = 0; m < 4; ++m)
; #pragma unroll
;                     for (int n = 0; n < 2; ++n) acc[a][b][m][n] = (f32x4){0.f, 0.f, 0.f, 0.f}; }
.LBB0_300:
	s_add_i32 s16, s16, s100
	s_cmp_ge_i32 s16, 46
	s_cselect_b32 s101, 46, 0
	s_sub_i32 s16, s16, s101
	s_ashr_i32 s19, s18, 31
	s_lshl_b64 s[54:55], s[18:19], 20
	s_add_u32 s54, s6, s54
	s_addc_u32 s55, s7, s55
	v_readlane_b32 vcc_lo, v253, 2
	s_and_b32 vcc_lo, vcc_lo, 7
	s_lshl_b32 vcc_hi, vcc_lo, 1
	s_sub_i32 s99, 28, vcc_hi
	s_lshl_b32 vcc_lo, vcc_lo, 8
	s_add_u32 s54, s54, vcc_lo
	s_addc_u32 s55, s55, 0
	s_and_b64 s[56:57], s[4:5], exec
	s_cselect_b32 s19, s55, s61
	s_cselect_b32 s62, s54, s60
	s_ashr_i32 s17, s16, 31
	s_lshl_b64 s[56:57], s[16:17], 20
	s_add_u32 s56, s3, s56
	s_addc_u32 s57, s20, s57
	s_add_u32 s56, s56, vcc_lo
	s_addc_u32 s57, s57, 0
	s_and_b64 s[66:67], s[4:5], exec
	s_cselect_b32 s17, s57, s65
	s_cselect_b32 s63, s56, s64
	s_add_u32 s66, s64, 0x100
	v_mov_b32_e32 v2, 0
	s_addc_u32 s67, s65, 0
	s_mov_b32 s68, -2
	v_mov_b32_e32 v3, v2
	v_mov_b32_e32 v4, v2
	v_mov_b32_e32 v5, v2
	v_mov_b32_e32 v6, v2
	v_mov_b32_e32 v7, v2
	v_mov_b32_e32 v8, v2
	v_mov_b32_e32 v9, v2
	v_mov_b32_e32 v14, v2
	v_mov_b32_e32 v15, v2
	v_mov_b32_e32 v16, v2
	v_mov_b32_e32 v17, v2
	v_mov_b32_e32 v22, v2
	v_mov_b32_e32 v23, v2
	v_mov_b32_e32 v24, v2
	v_mov_b32_e32 v25, v2
	v_mov_b32_e32 v30, v2
	v_mov_b32_e32 v31, v2
	v_mov_b32_e32 v32, v2
	v_mov_b32_e32 v33, v2
	v_mov_b32_e32 v38, v2
	v_mov_b32_e32 v39, v2
	v_mov_b32_e32 v40, v2
	v_mov_b32_e32 v41, v2
	v_mov_b32_e32 v46, v2
	v_mov_b32_e32 v47, v2
	v_mov_b32_e32 v48, v2
	v_mov_b32_e32 v49, v2
	v_mov_b32_e32 v54, v2
	v_mov_b32_e32 v55, v2
	v_mov_b32_e32 v56, v2
	v_mov_b32_e32 v57, v2
	v_mov_b32_e32 v10, v2
	v_mov_b32_e32 v11, v2
	v_mov_b32_e32 v12, v2
	v_mov_b32_e32 v13, v2
	v_mov_b32_e32 v18, v2
	v_mov_b32_e32 v19, v2
	v_mov_b32_e32 v20, v2
	v_mov_b32_e32 v21, v2
	v_mov_b32_e32 v26, v2
	v_mov_b32_e32 v27, v2
	v_mov_b32_e32 v28, v2
	v_mov_b32_e32 v29, v2
	v_mov_b32_e32 v34, v2
	v_mov_b32_e32 v35, v2
	v_mov_b32_e32 v36, v2
	v_mov_b32_e32 v37, v2
	v_mov_b32_e32 v42, v2
	v_mov_b32_e32 v43, v2
	v_mov_b32_e32 v44, v2
	v_mov_b32_e32 v45, v2
	v_mov_b32_e32 v50, v2
	v_mov_b32_e32 v51, v2
	v_mov_b32_e32 v52, v2
	v_mov_b32_e32 v53, v2
	v_mov_b32_e32 v58, v2
	v_mov_b32_e32 v59, v2
	v_mov_b32_e32 v60, v2
	v_mov_b32_e32 v61, v2
	v_mov_b32_e32 v62, v2
	v_mov_b32_e32 v63, v2
	v_mov_b32_e32 v64, v2
	v_mov_b32_e32 v65, v2
	v_mov_b32_e32 v66, v2
	v_mov_b32_e32 v67, v2
	v_mov_b32_e32 v68, v2
	v_mov_b32_e32 v69, v2
	v_mov_b32_e32 v70, v2
	v_mov_b32_e32 v71, v2
	v_mov_b32_e32 v72, v2
	v_mov_b32_e32 v73, v2
	v_mov_b32_e32 v78, v2
	v_mov_b32_e32 v79, v2
	v_mov_b32_e32 v80, v2
	v_mov_b32_e32 v81, v2
	v_mov_b32_e32 v86, v2
	v_mov_b32_e32 v87, v2
	v_mov_b32_e32 v88, v2
	v_mov_b32_e32 v89, v2
	v_mov_b32_e32 v94, v2
	v_mov_b32_e32 v95, v2
	v_mov_b32_e32 v96, v2
	v_mov_b32_e32 v97, v2
	v_mov_b32_e32 v102, v2
	v_mov_b32_e32 v103, v2
	v_mov_b32_e32 v104, v2
	v_mov_b32_e32 v105, v2
	v_mov_b32_e32 v110, v2
	v_mov_b32_e32 v111, v2
	v_mov_b32_e32 v112, v2
	v_mov_b32_e32 v113, v2
	v_mov_b32_e32 v118, v2
	v_mov_b32_e32 v119, v2
	v_mov_b32_e32 v120, v2
	v_mov_b32_e32 v121, v2
	v_mov_b32_e32 v74, v2
	v_mov_b32_e32 v75, v2
	v_mov_b32_e32 v76, v2
	v_mov_b32_e32 v77, v2
	v_mov_b32_e32 v82, v2
	v_mov_b32_e32 v83, v2
	v_mov_b32_e32 v84, v2
	v_mov_b32_e32 v85, v2
	v_mov_b32_e32 v90, v2
	v_mov_b32_e32 v91, v2
	v_mov_b32_e32 v92, v2
	v_mov_b32_e32 v93, v2
	v_mov_b32_e32 v98, v2
	v_mov_b32_e32 v99, v2
	v_mov_b32_e32 v100, v2
	v_mov_b32_e32 v101, v2
	v_mov_b32_e32 v106, v2
	v_mov_b32_e32 v107, v2
	v_mov_b32_e32 v108, v2
	v_mov_b32_e32 v109, v2
	v_mov_b32_e32 v114, v2
	v_mov_b32_e32 v115, v2
	v_mov_b32_e32 v116, v2
	v_mov_b32_e32 v117, v2
	v_mov_b32_e32 v122, v2
	v_mov_b32_e32 v123, v2
	v_mov_b32_e32 v124, v2
	v_mov_b32_e32 v125, v2
	v_mov_b32_e32 v126, v2
	v_mov_b32_e32 v127, v2
	v_mov_b32_e32 v128, v2
	v_mov_b32_e32 v129, v2
